# v035-packed-u16-histogram-table
# speedup vs baseline: 1.0072x; 1.0072x over previous
.LBB0_31:
	s_or_b64 exec, exec, s[4:5]
	s_movk_i32 s3, 0xc4
	v_cmp_gt_u32_e32 vcc, s3, v0
	s_waitcnt lgkmcnt(0)
	s_barrier
	s_and_saveexec_b64 s[4:5], vcc
	s_cbranch_execz .LBB0_36
	v_lshlrev_b32_e32 v1, 3, v0
	ds_read_b64 v[2:3], v1
	s_mul_i32 s3, s2, 0xc4
	v_add_u32_e32 v4, s3, v0
	v_mov_b32_e32 v5, 0
	v_lshl_add_u64 v[6:7], v[4:5], 2, s[10:11]
	s_movk_i32 s3, 0xc3
	v_cmp_ne_u32_e32 vcc, s3, v0
	s_waitcnt lgkmcnt(0)
	s_nop 0
	v_cndmask_b32_e32 v3, 0, v3, vcc
	v_lshl_or_b32 v2, v3, 16, v2
	global_store_dword v[6:7], v2, off

.LBB1_20:
	s_or_b64 exec, exec, s[4:5]
	v_and_b32_e32 v10, 0x7f, v0
	s_movk_i32 s3, 0x31
	v_cmp_gt_u32_e32 vcc, s3, v10
	s_and_saveexec_b64 s[6:7], vcc
	s_cbranch_execz .LBB1_22
	s_load_dwordx2 s[4:5], s[0:1], 0x18
	v_lshrrev_b32_e32 v25, 7, v0
	v_lshlrev_b32_e32 v29, 5, v10
	v_lshlrev_b32_e32 v28, 4, v10
	s_movk_i32 s3, 0x620
	v_readfirstlane_b32 s12, v0
	v_mad_u32_u24 v25, v25, s3, v29
	s_lshr_b32 s12, s12, 7
	s_lshl_b32 s13, s12, 6
	s_mul_i32 s14, s13, 0x310
	s_sub_i32 s15, s2, s13
	v_mov_b32_e32 v30, 0
	v_mov_b32_e32 v31, 0
	v_mov_b32_e32 v32, 0
	v_mov_b32_e32 v33, 0
	v_mov_b32_e32 v34, 0
	v_mov_b32_e32 v35, 0
	v_mov_b32_e32 v36, 0
	v_mov_b32_e32 v37, 0
	v_mov_b32_e32 v38, 0
	v_mov_b32_e32 v39, 0
	v_mov_b32_e32 v40, 0
	v_mov_b32_e32 v41, 0
	v_mov_b32_e32 v42, 0
	v_mov_b32_e32 v43, 0
	v_mov_b32_e32 v44, 0
	v_mov_b32_e32 v45, 0
	s_waitcnt lgkmcnt(0)
	s_add_u32 s4, s4, s14
	s_addc_u32 s5, s5, 0
	global_load_dwordx4 v[68:71], v28, s[4:5]
	global_load_dwordx4 v[72:75], v28, s[4:5] offset:784
	global_load_dwordx4 v[76:79], v28, s[4:5] offset:1568
	global_load_dwordx4 v[80:83], v28, s[4:5] offset:2352
	global_load_dwordx4 v[84:87], v28, s[4:5] offset:3136
	s_add_u32 s4, s4, 0xf50
	s_addc_u32 s5, s5, 0
	global_load_dwordx4 v[88:91], v28, s[4:5]
	global_load_dwordx4 v[92:95], v28, s[4:5] offset:784
	global_load_dwordx4 v[96:99], v28, s[4:5] offset:1568
	global_load_dwordx4 v[100:103], v28, s[4:5] offset:2352
	global_load_dwordx4 v[104:107], v28, s[4:5] offset:3136
	s_add_u32 s4, s4, 0xf50
	s_addc_u32 s5, s5, 0
	global_load_dwordx4 v[108:111], v28, s[4:5]
	global_load_dwordx4 v[112:115], v28, s[4:5] offset:784
	global_load_dwordx4 v[116:119], v28, s[4:5] offset:1568
	global_load_dwordx4 v[120:123], v28, s[4:5] offset:2352
	global_load_dwordx4 v[124:127], v28, s[4:5] offset:3136
	s_add_u32 s4, s4, 0xf50
	s_addc_u32 s5, s5, 0
	global_load_dwordx4 v[128:131], v28, s[4:5]
	global_load_dwordx4 v[132:135], v28, s[4:5] offset:784
	global_load_dwordx4 v[136:139], v28, s[4:5] offset:1568
	global_load_dwordx4 v[140:143], v28, s[4:5] offset:2352
	global_load_dwordx4 v[144:147], v28, s[4:5] offset:3136
	s_add_u32 s4, s4, 0xf50
	s_addc_u32 s5, s5, 0
	global_load_dwordx4 v[148:151], v28, s[4:5]
	global_load_dwordx4 v[152:155], v28, s[4:5] offset:784
	global_load_dwordx4 v[156:159], v28, s[4:5] offset:1568
	global_load_dwordx4 v[160:163], v28, s[4:5] offset:2352
	global_load_dwordx4 v[164:167], v28, s[4:5] offset:3136
	s_add_u32 s4, s4, 0xf50
	s_addc_u32 s5, s5, 0
	global_load_dwordx4 v[168:171], v28, s[4:5]
	global_load_dwordx4 v[172:175], v28, s[4:5] offset:784
	global_load_dwordx4 v[176:179], v28, s[4:5] offset:1568
	global_load_dwordx4 v[180:183], v28, s[4:5] offset:2352
	global_load_dwordx4 v[184:187], v28, s[4:5] offset:3136
	s_add_u32 s4, s4, 0xf50
	s_addc_u32 s5, s5, 0
	global_load_dwordx4 v[188:191], v28, s[4:5]
	global_load_dwordx4 v[192:195], v28, s[4:5] offset:784
	s_waitcnt vmcnt(0)
	v_add3_u32 v46, v68, v72, v76
	v_add3_u32 v46, v46, v80, v84
	v_add3_u32 v46, v46, v88, v92
	v_add3_u32 v46, v46, v96, v100
	v_add3_u32 v46, v46, v104, v108
	v_add3_u32 v46, v46, v112, v116
	v_add3_u32 v46, v46, v120, v124
	v_add_u32_e32 v46, v46, v128
	v_add3_u32 v47, v69, v73, v77
	v_add3_u32 v47, v47, v81, v85
	v_add3_u32 v47, v47, v89, v93
	v_add3_u32 v47, v47, v97, v101
	v_add3_u32 v47, v47, v105, v109
	v_add3_u32 v47, v47, v113, v117
	v_add3_u32 v47, v47, v121, v125
	v_add_u32_e32 v47, v47, v129
	v_add3_u32 v48, v70, v74, v78
	v_add3_u32 v48, v48, v82, v86
	v_add3_u32 v48, v48, v90, v94
	v_add3_u32 v48, v48, v98, v102
	v_add3_u32 v48, v48, v106, v110
	v_add3_u32 v48, v48, v114, v118
	v_add3_u32 v48, v48, v122, v126
	v_add_u32_e32 v48, v48, v130
	v_add3_u32 v49, v71, v75, v79
	v_add3_u32 v49, v49, v83, v87
	v_add3_u32 v49, v49, v91, v95
	v_add3_u32 v49, v49, v99, v103
	v_add3_u32 v49, v49, v107, v111
	v_add3_u32 v49, v49, v115, v119
	v_add3_u32 v49, v49, v123, v127
	v_add_u32_e32 v49, v49, v131
	v_and_b32_e32 v50, 0xffff, v46
	v_lshrrev_b32_e32 v51, 16, v46
	v_and_b32_e32 v52, 0xffff, v47
	v_lshrrev_b32_e32 v53, 16, v47
	v_and_b32_e32 v54, 0xffff, v48
	v_lshrrev_b32_e32 v55, 16, v48
	v_and_b32_e32 v56, 0xffff, v49
	v_lshrrev_b32_e32 v57, 16, v49
	v_add_u32_e32 v30, v30, v50
	v_add_u32_e32 v31, v31, v51
	v_add_u32_e32 v32, v32, v52
	v_add_u32_e32 v33, v33, v53
	v_add_u32_e32 v34, v34, v54
	v_add_u32_e32 v35, v35, v55
	v_add_u32_e32 v36, v36, v56
	v_add_u32_e32 v37, v37, v57
	s_cmp_ge_i32 s15, 16
	s_cbranch_scc0 .Lbscat_nf_0
	v_add_u32_e32 v38, v38, v50
	v_add_u32_e32 v39, v39, v51
	v_add_u32_e32 v40, v40, v52
	v_add_u32_e32 v41, v41, v53
	v_add_u32_e32 v42, v42, v54
	v_add_u32_e32 v43, v43, v55
	v_add_u32_e32 v44, v44, v56
	v_add_u32_e32 v45, v45, v57
	s_branch .Lbscat_dn_0
.Lbscat_nf_0:
	s_cmp_gt_i32 s15, 0
	s_cbranch_scc0 .Lbscat_dn_0
	v_mov_b32_e32 v58, 0
	v_mov_b32_e32 v59, 0
	v_mov_b32_e32 v60, 0
	v_mov_b32_e32 v61, 0
	s_cmp_gt_i32 s15, 0
	s_cselect_b32 s16, -1, 0
	v_and_b32_e32 v62, s16, v68
	v_add_u32_e32 v58, v58, v62
	v_and_b32_e32 v62, s16, v69
	v_add_u32_e32 v59, v59, v62
	v_and_b32_e32 v62, s16, v70
	v_add_u32_e32 v60, v60, v62
	v_and_b32_e32 v62, s16, v71
	v_add_u32_e32 v61, v61, v62
	s_cmp_gt_i32 s15, 1
	s_cselect_b32 s16, -1, 0
	v_and_b32_e32 v62, s16, v72
	v_add_u32_e32 v58, v58, v62
	v_and_b32_e32 v62, s16, v73
	v_add_u32_e32 v59, v59, v62
	v_and_b32_e32 v62, s16, v74
	v_add_u32_e32 v60, v60, v62
	v_and_b32_e32 v62, s16, v75
	v_add_u32_e32 v61, v61, v62
	s_cmp_gt_i32 s15, 2
	s_cselect_b32 s16, -1, 0
	v_and_b32_e32 v62, s16, v76
	v_add_u32_e32 v58, v58, v62
	v_and_b32_e32 v62, s16, v77
	v_add_u32_e32 v59, v59, v62
	v_and_b32_e32 v62, s16, v78
	v_add_u32_e32 v60, v60, v62
	v_and_b32_e32 v62, s16, v79
	v_add_u32_e32 v61, v61, v62
	s_cmp_gt_i32 s15, 3
	s_cselect_b32 s16, -1, 0
	v_and_b32_e32 v62, s16, v80
	v_add_u32_e32 v58, v58, v62
	v_and_b32_e32 v62, s16, v81
	v_add_u32_e32 v59, v59, v62
	v_and_b32_e32 v62, s16, v82
	v_add_u32_e32 v60, v60, v62
	v_and_b32_e32 v62, s16, v83
	v_add_u32_e32 v61, v61, v62
	s_cmp_gt_i32 s15, 4
	s_cselect_b32 s16, -1, 0
	v_and_b32_e32 v62, s16, v84
	v_add_u32_e32 v58, v58, v62
	v_and_b32_e32 v62, s16, v85
	v_add_u32_e32 v59, v59, v62
	v_and_b32_e32 v62, s16, v86
	v_add_u32_e32 v60, v60, v62
	v_and_b32_e32 v62, s16, v87
	v_add_u32_e32 v61, v61, v62
	s_cmp_gt_i32 s15, 5
	s_cselect_b32 s16, -1, 0
	v_and_b32_e32 v62, s16, v88
	v_add_u32_e32 v58, v58, v62
	v_and_b32_e32 v62, s16, v89
	v_add_u32_e32 v59, v59, v62
	v_and_b32_e32 v62, s16, v90
	v_add_u32_e32 v60, v60, v62
	v_and_b32_e32 v62, s16, v91
	v_add_u32_e32 v61, v61, v62
	s_cmp_gt_i32 s15, 6
	s_cselect_b32 s16, -1, 0
	v_and_b32_e32 v62, s16, v92
	v_add_u32_e32 v58, v58, v62
	v_and_b32_e32 v62, s16, v93
	v_add_u32_e32 v59, v59, v62
	v_and_b32_e32 v62, s16, v94
	v_add_u32_e32 v60, v60, v62
	v_and_b32_e32 v62, s16, v95
	v_add_u32_e32 v61, v61, v62
	s_cmp_gt_i32 s15, 7
	s_cselect_b32 s16, -1, 0
	v_and_b32_e32 v62, s16, v96
	v_add_u32_e32 v58, v58, v62
	v_and_b32_e32 v62, s16, v97
	v_add_u32_e32 v59, v59, v62
	v_and_b32_e32 v62, s16, v98
	v_add_u32_e32 v60, v60, v62
	v_and_b32_e32 v62, s16, v99
	v_add_u32_e32 v61, v61, v62
	s_cmp_gt_i32 s15, 8
	s_cselect_b32 s16, -1, 0
	v_and_b32_e32 v62, s16, v100
	v_add_u32_e32 v58, v58, v62
	v_and_b32_e32 v62, s16, v101
	v_add_u32_e32 v59, v59, v62
	v_and_b32_e32 v62, s16, v102
	v_add_u32_e32 v60, v60, v62
	v_and_b32_e32 v62, s16, v103
	v_add_u32_e32 v61, v61, v62
	s_cmp_gt_i32 s15, 9
	s_cselect_b32 s16, -1, 0
	v_and_b32_e32 v62, s16, v104
	v_add_u32_e32 v58, v58, v62
	v_and_b32_e32 v62, s16, v105
	v_add_u32_e32 v59, v59, v62
	v_and_b32_e32 v62, s16, v106
	v_add_u32_e32 v60, v60, v62
	v_and_b32_e32 v62, s16, v107
	v_add_u32_e32 v61, v61, v62
	s_cmp_gt_i32 s15, 10
	s_cselect_b32 s16, -1, 0
	v_and_b32_e32 v62, s16, v108
	v_add_u32_e32 v58, v58, v62
	v_and_b32_e32 v62, s16, v109
	v_add_u32_e32 v59, v59, v62
	v_and_b32_e32 v62, s16, v110
	v_add_u32_e32 v60, v60, v62
	v_and_b32_e32 v62, s16, v111
	v_add_u32_e32 v61, v61, v62
	s_cmp_gt_i32 s15, 11
	s_cselect_b32 s16, -1, 0
	v_and_b32_e32 v62, s16, v112
	v_add_u32_e32 v58, v58, v62
	v_and_b32_e32 v62, s16, v113
	v_add_u32_e32 v59, v59, v62
	v_and_b32_e32 v62, s16, v114
	v_add_u32_e32 v60, v60, v62
	v_and_b32_e32 v62, s16, v115
	v_add_u32_e32 v61, v61, v62
	s_cmp_gt_i32 s15, 12
	s_cselect_b32 s16, -1, 0
	v_and_b32_e32 v62, s16, v116
	v_add_u32_e32 v58, v58, v62
	v_and_b32_e32 v62, s16, v117
	v_add_u32_e32 v59, v59, v62
	v_and_b32_e32 v62, s16, v118
	v_add_u32_e32 v60, v60, v62
	v_and_b32_e32 v62, s16, v119
	v_add_u32_e32 v61, v61, v62
	s_cmp_gt_i32 s15, 13
	s_cselect_b32 s16, -1, 0
	v_and_b32_e32 v62, s16, v120
	v_add_u32_e32 v58, v58, v62
	v_and_b32_e32 v62, s16, v121
	v_add_u32_e32 v59, v59, v62
	v_and_b32_e32 v62, s16, v122
	v_add_u32_e32 v60, v60, v62
	v_and_b32_e32 v62, s16, v123
	v_add_u32_e32 v61, v61, v62
	s_cmp_gt_i32 s15, 14
	s_cselect_b32 s16, -1, 0
	v_and_b32_e32 v62, s16, v124
	v_add_u32_e32 v58, v58, v62
	v_and_b32_e32 v62, s16, v125
	v_add_u32_e32 v59, v59, v62
	v_and_b32_e32 v62, s16, v126
	v_add_u32_e32 v60, v60, v62
	v_and_b32_e32 v62, s16, v127
	v_add_u32_e32 v61, v61, v62
	s_cmp_gt_i32 s15, 15
	s_cselect_b32 s16, -1, 0
	v_and_b32_e32 v62, s16, v128
	v_add_u32_e32 v58, v58, v62
	v_and_b32_e32 v62, s16, v129
	v_add_u32_e32 v59, v59, v62
	v_and_b32_e32 v62, s16, v130
	v_add_u32_e32 v60, v60, v62
	v_and_b32_e32 v62, s16, v131
	v_add_u32_e32 v61, v61, v62
	v_and_b32_e32 v50, 0xffff, v58
	v_lshrrev_b32_e32 v51, 16, v58
	v_and_b32_e32 v52, 0xffff, v59
	v_lshrrev_b32_e32 v53, 16, v59
	v_and_b32_e32 v54, 0xffff, v60
	v_lshrrev_b32_e32 v55, 16, v60
	v_and_b32_e32 v56, 0xffff, v61
	v_lshrrev_b32_e32 v57, 16, v61
	v_add_u32_e32 v38, v38, v50
	v_add_u32_e32 v39, v39, v51
	v_add_u32_e32 v40, v40, v52
	v_add_u32_e32 v41, v41, v53
	v_add_u32_e32 v42, v42, v54
	v_add_u32_e32 v43, v43, v55
	v_add_u32_e32 v44, v44, v56
	v_add_u32_e32 v45, v45, v57
.Lbscat_dn_0:
	v_add3_u32 v46, v132, v136, v140
	v_add3_u32 v46, v46, v144, v148
	v_add3_u32 v46, v46, v152, v156
	v_add3_u32 v46, v46, v160, v164
	v_add3_u32 v46, v46, v168, v172
	v_add3_u32 v46, v46, v176, v180
	v_add3_u32 v46, v46, v184, v188
	v_add_u32_e32 v46, v46, v192
	v_add3_u32 v47, v133, v137, v141
	v_add3_u32 v47, v47, v145, v149
	v_add3_u32 v47, v47, v153, v157
	v_add3_u32 v47, v47, v161, v165
	v_add3_u32 v47, v47, v169, v173
	v_add3_u32 v47, v47, v177, v181
	v_add3_u32 v47, v47, v185, v189
	v_add_u32_e32 v47, v47, v193
	v_add3_u32 v48, v134, v138, v142
	v_add3_u32 v48, v48, v146, v150
	v_add3_u32 v48, v48, v154, v158
	v_add3_u32 v48, v48, v162, v166
	v_add3_u32 v48, v48, v170, v174
	v_add3_u32 v48, v48, v178, v182
	v_add3_u32 v48, v48, v186, v190
	v_add_u32_e32 v48, v48, v194
	v_add3_u32 v49, v135, v139, v143
	v_add3_u32 v49, v49, v147, v151
	v_add3_u32 v49, v49, v155, v159
	v_add3_u32 v49, v49, v163, v167
	v_add3_u32 v49, v49, v171, v175
	v_add3_u32 v49, v49, v179, v183
	v_add3_u32 v49, v49, v187, v191
	v_add_u32_e32 v49, v49, v195
	v_and_b32_e32 v50, 0xffff, v46
	v_lshrrev_b32_e32 v51, 16, v46
	v_and_b32_e32 v52, 0xffff, v47
	v_lshrrev_b32_e32 v53, 16, v47
	v_and_b32_e32 v54, 0xffff, v48
	v_lshrrev_b32_e32 v55, 16, v48
	v_and_b32_e32 v56, 0xffff, v49
	v_lshrrev_b32_e32 v57, 16, v49
	v_add_u32_e32 v30, v30, v50
	v_add_u32_e32 v31, v31, v51
	v_add_u32_e32 v32, v32, v52
	v_add_u32_e32 v33, v33, v53
	v_add_u32_e32 v34, v34, v54
	v_add_u32_e32 v35, v35, v55
	v_add_u32_e32 v36, v36, v56
	v_add_u32_e32 v37, v37, v57
	s_cmp_ge_i32 s15, 32
	s_cbranch_scc0 .Lbscat_nf_1
	v_add_u32_e32 v38, v38, v50
	v_add_u32_e32 v39, v39, v51
	v_add_u32_e32 v40, v40, v52
	v_add_u32_e32 v41, v41, v53
	v_add_u32_e32 v42, v42, v54
	v_add_u32_e32 v43, v43, v55
	v_add_u32_e32 v44, v44, v56
	v_add_u32_e32 v45, v45, v57
	s_branch .Lbscat_dn_1
.Lbscat_nf_1:
	s_cmp_gt_i32 s15, 16
	s_cbranch_scc0 .Lbscat_dn_1
	v_mov_b32_e32 v58, 0
	v_mov_b32_e32 v59, 0
	v_mov_b32_e32 v60, 0
	v_mov_b32_e32 v61, 0
	s_cmp_gt_i32 s15, 16
	s_cselect_b32 s16, -1, 0
	v_and_b32_e32 v62, s16, v132
	v_add_u32_e32 v58, v58, v62
	v_and_b32_e32 v62, s16, v133
	v_add_u32_e32 v59, v59, v62
	v_and_b32_e32 v62, s16, v134
	v_add_u32_e32 v60, v60, v62
	v_and_b32_e32 v62, s16, v135
	v_add_u32_e32 v61, v61, v62
	s_cmp_gt_i32 s15, 17
	s_cselect_b32 s16, -1, 0
	v_and_b32_e32 v62, s16, v136
	v_add_u32_e32 v58, v58, v62
	v_and_b32_e32 v62, s16, v137
	v_add_u32_e32 v59, v59, v62
	v_and_b32_e32 v62, s16, v138
	v_add_u32_e32 v60, v60, v62
	v_and_b32_e32 v62, s16, v139
	v_add_u32_e32 v61, v61, v62
	s_cmp_gt_i32 s15, 18
	s_cselect_b32 s16, -1, 0
	v_and_b32_e32 v62, s16, v140
	v_add_u32_e32 v58, v58, v62
	v_and_b32_e32 v62, s16, v141
	v_add_u32_e32 v59, v59, v62
	v_and_b32_e32 v62, s16, v142
	v_add_u32_e32 v60, v60, v62
	v_and_b32_e32 v62, s16, v143
	v_add_u32_e32 v61, v61, v62
	s_cmp_gt_i32 s15, 19
	s_cselect_b32 s16, -1, 0
	v_and_b32_e32 v62, s16, v144
	v_add_u32_e32 v58, v58, v62
	v_and_b32_e32 v62, s16, v145
	v_add_u32_e32 v59, v59, v62
	v_and_b32_e32 v62, s16, v146
	v_add_u32_e32 v60, v60, v62
	v_and_b32_e32 v62, s16, v147
	v_add_u32_e32 v61, v61, v62
	s_cmp_gt_i32 s15, 20
	s_cselect_b32 s16, -1, 0
	v_and_b32_e32 v62, s16, v148
	v_add_u32_e32 v58, v58, v62
	v_and_b32_e32 v62, s16, v149
	v_add_u32_e32 v59, v59, v62
	v_and_b32_e32 v62, s16, v150
	v_add_u32_e32 v60, v60, v62
	v_and_b32_e32 v62, s16, v151
	v_add_u32_e32 v61, v61, v62
	s_cmp_gt_i32 s15, 21
	s_cselect_b32 s16, -1, 0
	v_and_b32_e32 v62, s16, v152
	v_add_u32_e32 v58, v58, v62
	v_and_b32_e32 v62, s16, v153
	v_add_u32_e32 v59, v59, v62
	v_and_b32_e32 v62, s16, v154
	v_add_u32_e32 v60, v60, v62
	v_and_b32_e32 v62, s16, v155
	v_add_u32_e32 v61, v61, v62
	s_cmp_gt_i32 s15, 22
	s_cselect_b32 s16, -1, 0
	v_and_b32_e32 v62, s16, v156
	v_add_u32_e32 v58, v58, v62
	v_and_b32_e32 v62, s16, v157
	v_add_u32_e32 v59, v59, v62
	v_and_b32_e32 v62, s16, v158
	v_add_u32_e32 v60, v60, v62
	v_and_b32_e32 v62, s16, v159
	v_add_u32_e32 v61, v61, v62
	s_cmp_gt_i32 s15, 23
	s_cselect_b32 s16, -1, 0
	v_and_b32_e32 v62, s16, v160
	v_add_u32_e32 v58, v58, v62
	v_and_b32_e32 v62, s16, v161
	v_add_u32_e32 v59, v59, v62
	v_and_b32_e32 v62, s16, v162
	v_add_u32_e32 v60, v60, v62
	v_and_b32_e32 v62, s16, v163
	v_add_u32_e32 v61, v61, v62
	s_cmp_gt_i32 s15, 24
	s_cselect_b32 s16, -1, 0
	v_and_b32_e32 v62, s16, v164
	v_add_u32_e32 v58, v58, v62
	v_and_b32_e32 v62, s16, v165
	v_add_u32_e32 v59, v59, v62
	v_and_b32_e32 v62, s16, v166
	v_add_u32_e32 v60, v60, v62
	v_and_b32_e32 v62, s16, v167
	v_add_u32_e32 v61, v61, v62
	s_cmp_gt_i32 s15, 25
	s_cselect_b32 s16, -1, 0
	v_and_b32_e32 v62, s16, v168
	v_add_u32_e32 v58, v58, v62
	v_and_b32_e32 v62, s16, v169
	v_add_u32_e32 v59, v59, v62
	v_and_b32_e32 v62, s16, v170
	v_add_u32_e32 v60, v60, v62
	v_and_b32_e32 v62, s16, v171
	v_add_u32_e32 v61, v61, v62
	s_cmp_gt_i32 s15, 26
	s_cselect_b32 s16, -1, 0
	v_and_b32_e32 v62, s16, v172
	v_add_u32_e32 v58, v58, v62
	v_and_b32_e32 v62, s16, v173
	v_add_u32_e32 v59, v59, v62
	v_and_b32_e32 v62, s16, v174
	v_add_u32_e32 v60, v60, v62
	v_and_b32_e32 v62, s16, v175
	v_add_u32_e32 v61, v61, v62
	s_cmp_gt_i32 s15, 27
	s_cselect_b32 s16, -1, 0
	v_and_b32_e32 v62, s16, v176
	v_add_u32_e32 v58, v58, v62
	v_and_b32_e32 v62, s16, v177
	v_add_u32_e32 v59, v59, v62
	v_and_b32_e32 v62, s16, v178
	v_add_u32_e32 v60, v60, v62
	v_and_b32_e32 v62, s16, v179
	v_add_u32_e32 v61, v61, v62
	s_cmp_gt_i32 s15, 28
	s_cselect_b32 s16, -1, 0
	v_and_b32_e32 v62, s16, v180
	v_add_u32_e32 v58, v58, v62
	v_and_b32_e32 v62, s16, v181
	v_add_u32_e32 v59, v59, v62
	v_and_b32_e32 v62, s16, v182
	v_add_u32_e32 v60, v60, v62
	v_and_b32_e32 v62, s16, v183
	v_add_u32_e32 v61, v61, v62
	s_cmp_gt_i32 s15, 29
	s_cselect_b32 s16, -1, 0
	v_and_b32_e32 v62, s16, v184
	v_add_u32_e32 v58, v58, v62
	v_and_b32_e32 v62, s16, v185
	v_add_u32_e32 v59, v59, v62
	v_and_b32_e32 v62, s16, v186
	v_add_u32_e32 v60, v60, v62
	v_and_b32_e32 v62, s16, v187
	v_add_u32_e32 v61, v61, v62
	s_cmp_gt_i32 s15, 30
	s_cselect_b32 s16, -1, 0
	v_and_b32_e32 v62, s16, v188
	v_add_u32_e32 v58, v58, v62
	v_and_b32_e32 v62, s16, v189
	v_add_u32_e32 v59, v59, v62
	v_and_b32_e32 v62, s16, v190
	v_add_u32_e32 v60, v60, v62
	v_and_b32_e32 v62, s16, v191
	v_add_u32_e32 v61, v61, v62
	s_cmp_gt_i32 s15, 31
	s_cselect_b32 s16, -1, 0
	v_and_b32_e32 v62, s16, v192
	v_add_u32_e32 v58, v58, v62
	v_and_b32_e32 v62, s16, v193
	v_add_u32_e32 v59, v59, v62
	v_and_b32_e32 v62, s16, v194
	v_add_u32_e32 v60, v60, v62
	v_and_b32_e32 v62, s16, v195
	v_add_u32_e32 v61, v61, v62
	v_and_b32_e32 v50, 0xffff, v58
	v_lshrrev_b32_e32 v51, 16, v58
	v_and_b32_e32 v52, 0xffff, v59
	v_lshrrev_b32_e32 v53, 16, v59
	v_and_b32_e32 v54, 0xffff, v60
	v_lshrrev_b32_e32 v55, 16, v60
	v_and_b32_e32 v56, 0xffff, v61
	v_lshrrev_b32_e32 v57, 16, v61
	v_add_u32_e32 v38, v38, v50
	v_add_u32_e32 v39, v39, v51
	v_add_u32_e32 v40, v40, v52
	v_add_u32_e32 v41, v41, v53
	v_add_u32_e32 v42, v42, v54
	v_add_u32_e32 v43, v43, v55
	v_add_u32_e32 v44, v44, v56
	v_add_u32_e32 v45, v45, v57
.Lbscat_dn_1:
	global_load_dwordx4 v[68:71], v28, s[4:5] offset:1568
	global_load_dwordx4 v[72:75], v28, s[4:5] offset:2352
	global_load_dwordx4 v[76:79], v28, s[4:5] offset:3136
	s_add_u32 s4, s4, 0xf50
	s_addc_u32 s5, s5, 0
	global_load_dwordx4 v[80:83], v28, s[4:5]
	global_load_dwordx4 v[84:87], v28, s[4:5] offset:784
	global_load_dwordx4 v[88:91], v28, s[4:5] offset:1568
	global_load_dwordx4 v[92:95], v28, s[4:5] offset:2352
	global_load_dwordx4 v[96:99], v28, s[4:5] offset:3136
	s_add_u32 s4, s4, 0xf50
	s_addc_u32 s5, s5, 0
	global_load_dwordx4 v[100:103], v28, s[4:5]
	global_load_dwordx4 v[104:107], v28, s[4:5] offset:784
	global_load_dwordx4 v[108:111], v28, s[4:5] offset:1568
	global_load_dwordx4 v[112:115], v28, s[4:5] offset:2352
	global_load_dwordx4 v[116:119], v28, s[4:5] offset:3136
	s_add_u32 s4, s4, 0xf50
	s_addc_u32 s5, s5, 0
	global_load_dwordx4 v[120:123], v28, s[4:5]
	global_load_dwordx4 v[124:127], v28, s[4:5] offset:784
	global_load_dwordx4 v[128:131], v28, s[4:5] offset:1568
	global_load_dwordx4 v[132:135], v28, s[4:5] offset:2352
	global_load_dwordx4 v[136:139], v28, s[4:5] offset:3136
	s_add_u32 s4, s4, 0xf50
	s_addc_u32 s5, s5, 0
	global_load_dwordx4 v[140:143], v28, s[4:5]
	global_load_dwordx4 v[144:147], v28, s[4:5] offset:784
	global_load_dwordx4 v[148:151], v28, s[4:5] offset:1568
	global_load_dwordx4 v[152:155], v28, s[4:5] offset:2352
	global_load_dwordx4 v[156:159], v28, s[4:5] offset:3136
	s_add_u32 s4, s4, 0xf50
	s_addc_u32 s5, s5, 0
	global_load_dwordx4 v[160:163], v28, s[4:5]
	global_load_dwordx4 v[164:167], v28, s[4:5] offset:784
	global_load_dwordx4 v[168:171], v28, s[4:5] offset:1568
	global_load_dwordx4 v[172:175], v28, s[4:5] offset:2352
	global_load_dwordx4 v[176:179], v28, s[4:5] offset:3136
	s_add_u32 s4, s4, 0xf50
	s_addc_u32 s5, s5, 0
	global_load_dwordx4 v[180:183], v28, s[4:5]
	global_load_dwordx4 v[184:187], v28, s[4:5] offset:784
	global_load_dwordx4 v[188:191], v28, s[4:5] offset:1568
	global_load_dwordx4 v[192:195], v28, s[4:5] offset:2352
	s_waitcnt vmcnt(0)
	v_add3_u32 v46, v68, v72, v76
	v_add3_u32 v46, v46, v80, v84
	v_add3_u32 v46, v46, v88, v92
	v_add3_u32 v46, v46, v96, v100
	v_add3_u32 v46, v46, v104, v108
	v_add3_u32 v46, v46, v112, v116
	v_add3_u32 v46, v46, v120, v124
	v_add_u32_e32 v46, v46, v128
	v_add3_u32 v47, v69, v73, v77
	v_add3_u32 v47, v47, v81, v85
	v_add3_u32 v47, v47, v89, v93
	v_add3_u32 v47, v47, v97, v101
	v_add3_u32 v47, v47, v105, v109
	v_add3_u32 v47, v47, v113, v117
	v_add3_u32 v47, v47, v121, v125
	v_add_u32_e32 v47, v47, v129
	v_add3_u32 v48, v70, v74, v78
	v_add3_u32 v48, v48, v82, v86
	v_add3_u32 v48, v48, v90, v94
	v_add3_u32 v48, v48, v98, v102
	v_add3_u32 v48, v48, v106, v110
	v_add3_u32 v48, v48, v114, v118
	v_add3_u32 v48, v48, v122, v126
	v_add_u32_e32 v48, v48, v130
	v_add3_u32 v49, v71, v75, v79
	v_add3_u32 v49, v49, v83, v87
	v_add3_u32 v49, v49, v91, v95
	v_add3_u32 v49, v49, v99, v103
	v_add3_u32 v49, v49, v107, v111
	v_add3_u32 v49, v49, v115, v119
	v_add3_u32 v49, v49, v123, v127
	v_add_u32_e32 v49, v49, v131
	v_and_b32_e32 v50, 0xffff, v46
	v_lshrrev_b32_e32 v51, 16, v46
	v_and_b32_e32 v52, 0xffff, v47
	v_lshrrev_b32_e32 v53, 16, v47
	v_and_b32_e32 v54, 0xffff, v48
	v_lshrrev_b32_e32 v55, 16, v48
	v_and_b32_e32 v56, 0xffff, v49
	v_lshrrev_b32_e32 v57, 16, v49
	v_add_u32_e32 v30, v30, v50
	v_add_u32_e32 v31, v31, v51
	v_add_u32_e32 v32, v32, v52
	v_add_u32_e32 v33, v33, v53
	v_add_u32_e32 v34, v34, v54
	v_add_u32_e32 v35, v35, v55
	v_add_u32_e32 v36, v36, v56
	v_add_u32_e32 v37, v37, v57
	s_cmp_ge_i32 s15, 48
	s_cbranch_scc0 .Lbscat_nf_2
	v_add_u32_e32 v38, v38, v50
	v_add_u32_e32 v39, v39, v51
	v_add_u32_e32 v40, v40, v52
	v_add_u32_e32 v41, v41, v53
	v_add_u32_e32 v42, v42, v54
	v_add_u32_e32 v43, v43, v55
	v_add_u32_e32 v44, v44, v56
	v_add_u32_e32 v45, v45, v57
	s_branch .Lbscat_dn_2
.Lbscat_nf_2:
	s_cmp_gt_i32 s15, 32
	s_cbranch_scc0 .Lbscat_dn_2
	v_mov_b32_e32 v58, 0
	v_mov_b32_e32 v59, 0
	v_mov_b32_e32 v60, 0
	v_mov_b32_e32 v61, 0
	s_cmp_gt_i32 s15, 32
	s_cselect_b32 s16, -1, 0
	v_and_b32_e32 v62, s16, v68
	v_add_u32_e32 v58, v58, v62
	v_and_b32_e32 v62, s16, v69
	v_add_u32_e32 v59, v59, v62
	v_and_b32_e32 v62, s16, v70
	v_add_u32_e32 v60, v60, v62
	v_and_b32_e32 v62, s16, v71
	v_add_u32_e32 v61, v61, v62
	s_cmp_gt_i32 s15, 33
	s_cselect_b32 s16, -1, 0
	v_and_b32_e32 v62, s16, v72
	v_add_u32_e32 v58, v58, v62
	v_and_b32_e32 v62, s16, v73
	v_add_u32_e32 v59, v59, v62
	v_and_b32_e32 v62, s16, v74
	v_add_u32_e32 v60, v60, v62
	v_and_b32_e32 v62, s16, v75
	v_add_u32_e32 v61, v61, v62
	s_cmp_gt_i32 s15, 34
	s_cselect_b32 s16, -1, 0
	v_and_b32_e32 v62, s16, v76
	v_add_u32_e32 v58, v58, v62
	v_and_b32_e32 v62, s16, v77
	v_add_u32_e32 v59, v59, v62
	v_and_b32_e32 v62, s16, v78
	v_add_u32_e32 v60, v60, v62
	v_and_b32_e32 v62, s16, v79
	v_add_u32_e32 v61, v61, v62
	s_cmp_gt_i32 s15, 35
	s_cselect_b32 s16, -1, 0
	v_and_b32_e32 v62, s16, v80
	v_add_u32_e32 v58, v58, v62
	v_and_b32_e32 v62, s16, v81
	v_add_u32_e32 v59, v59, v62
	v_and_b32_e32 v62, s16, v82
	v_add_u32_e32 v60, v60, v62
	v_and_b32_e32 v62, s16, v83
	v_add_u32_e32 v61, v61, v62
	s_cmp_gt_i32 s15, 36
	s_cselect_b32 s16, -1, 0
	v_and_b32_e32 v62, s16, v84
	v_add_u32_e32 v58, v58, v62
	v_and_b32_e32 v62, s16, v85
	v_add_u32_e32 v59, v59, v62
	v_and_b32_e32 v62, s16, v86
	v_add_u32_e32 v60, v60, v62
	v_and_b32_e32 v62, s16, v87
	v_add_u32_e32 v61, v61, v62
	s_cmp_gt_i32 s15, 37
	s_cselect_b32 s16, -1, 0
	v_and_b32_e32 v62, s16, v88
	v_add_u32_e32 v58, v58, v62
	v_and_b32_e32 v62, s16, v89
	v_add_u32_e32 v59, v59, v62
	v_and_b32_e32 v62, s16, v90
	v_add_u32_e32 v60, v60, v62
	v_and_b32_e32 v62, s16, v91
	v_add_u32_e32 v61, v61, v62
	s_cmp_gt_i32 s15, 38
	s_cselect_b32 s16, -1, 0
	v_and_b32_e32 v62, s16, v92
	v_add_u32_e32 v58, v58, v62
	v_and_b32_e32 v62, s16, v93
	v_add_u32_e32 v59, v59, v62
	v_and_b32_e32 v62, s16, v94
	v_add_u32_e32 v60, v60, v62
	v_and_b32_e32 v62, s16, v95
	v_add_u32_e32 v61, v61, v62
	s_cmp_gt_i32 s15, 39
	s_cselect_b32 s16, -1, 0
	v_and_b32_e32 v62, s16, v96
	v_add_u32_e32 v58, v58, v62
	v_and_b32_e32 v62, s16, v97
	v_add_u32_e32 v59, v59, v62
	v_and_b32_e32 v62, s16, v98
	v_add_u32_e32 v60, v60, v62
	v_and_b32_e32 v62, s16, v99
	v_add_u32_e32 v61, v61, v62
	s_cmp_gt_i32 s15, 40
	s_cselect_b32 s16, -1, 0
	v_and_b32_e32 v62, s16, v100
	v_add_u32_e32 v58, v58, v62
	v_and_b32_e32 v62, s16, v101
	v_add_u32_e32 v59, v59, v62
	v_and_b32_e32 v62, s16, v102
	v_add_u32_e32 v60, v60, v62
	v_and_b32_e32 v62, s16, v103
	v_add_u32_e32 v61, v61, v62
	s_cmp_gt_i32 s15, 41
	s_cselect_b32 s16, -1, 0
	v_and_b32_e32 v62, s16, v104
	v_add_u32_e32 v58, v58, v62
	v_and_b32_e32 v62, s16, v105
	v_add_u32_e32 v59, v59, v62
	v_and_b32_e32 v62, s16, v106
	v_add_u32_e32 v60, v60, v62
	v_and_b32_e32 v62, s16, v107
	v_add_u32_e32 v61, v61, v62
	s_cmp_gt_i32 s15, 42
	s_cselect_b32 s16, -1, 0
	v_and_b32_e32 v62, s16, v108
	v_add_u32_e32 v58, v58, v62
	v_and_b32_e32 v62, s16, v109
	v_add_u32_e32 v59, v59, v62
	v_and_b32_e32 v62, s16, v110
	v_add_u32_e32 v60, v60, v62
	v_and_b32_e32 v62, s16, v111
	v_add_u32_e32 v61, v61, v62
	s_cmp_gt_i32 s15, 43
	s_cselect_b32 s16, -1, 0
	v_and_b32_e32 v62, s16, v112
	v_add_u32_e32 v58, v58, v62
	v_and_b32_e32 v62, s16, v113
	v_add_u32_e32 v59, v59, v62
	v_and_b32_e32 v62, s16, v114
	v_add_u32_e32 v60, v60, v62
	v_and_b32_e32 v62, s16, v115
	v_add_u32_e32 v61, v61, v62
	s_cmp_gt_i32 s15, 44
	s_cselect_b32 s16, -1, 0
	v_and_b32_e32 v62, s16, v116
	v_add_u32_e32 v58, v58, v62
	v_and_b32_e32 v62, s16, v117
	v_add_u32_e32 v59, v59, v62
	v_and_b32_e32 v62, s16, v118
	v_add_u32_e32 v60, v60, v62
	v_and_b32_e32 v62, s16, v119
	v_add_u32_e32 v61, v61, v62
	s_cmp_gt_i32 s15, 45
	s_cselect_b32 s16, -1, 0
	v_and_b32_e32 v62, s16, v120
	v_add_u32_e32 v58, v58, v62
	v_and_b32_e32 v62, s16, v121
	v_add_u32_e32 v59, v59, v62
	v_and_b32_e32 v62, s16, v122
	v_add_u32_e32 v60, v60, v62
	v_and_b32_e32 v62, s16, v123
	v_add_u32_e32 v61, v61, v62
	s_cmp_gt_i32 s15, 46
	s_cselect_b32 s16, -1, 0
	v_and_b32_e32 v62, s16, v124
	v_add_u32_e32 v58, v58, v62
	v_and_b32_e32 v62, s16, v125
	v_add_u32_e32 v59, v59, v62
	v_and_b32_e32 v62, s16, v126
	v_add_u32_e32 v60, v60, v62
	v_and_b32_e32 v62, s16, v127
	v_add_u32_e32 v61, v61, v62
	s_cmp_gt_i32 s15, 47
	s_cselect_b32 s16, -1, 0
	v_and_b32_e32 v62, s16, v128
	v_add_u32_e32 v58, v58, v62
	v_and_b32_e32 v62, s16, v129
	v_add_u32_e32 v59, v59, v62
	v_and_b32_e32 v62, s16, v130
	v_add_u32_e32 v60, v60, v62
	v_and_b32_e32 v62, s16, v131
	v_add_u32_e32 v61, v61, v62
	v_and_b32_e32 v50, 0xffff, v58
	v_lshrrev_b32_e32 v51, 16, v58
	v_and_b32_e32 v52, 0xffff, v59
	v_lshrrev_b32_e32 v53, 16, v59
	v_and_b32_e32 v54, 0xffff, v60
	v_lshrrev_b32_e32 v55, 16, v60
	v_and_b32_e32 v56, 0xffff, v61
	v_lshrrev_b32_e32 v57, 16, v61
	v_add_u32_e32 v38, v38, v50
	v_add_u32_e32 v39, v39, v51
	v_add_u32_e32 v40, v40, v52
	v_add_u32_e32 v41, v41, v53
	v_add_u32_e32 v42, v42, v54
	v_add_u32_e32 v43, v43, v55
	v_add_u32_e32 v44, v44, v56
	v_add_u32_e32 v45, v45, v57
.Lbscat_dn_2:
	v_add3_u32 v46, v132, v136, v140
	v_add3_u32 v46, v46, v144, v148
	v_add3_u32 v46, v46, v152, v156
	v_add3_u32 v46, v46, v160, v164
	v_add3_u32 v46, v46, v168, v172
	v_add3_u32 v46, v46, v176, v180
	v_add3_u32 v46, v46, v184, v188
	v_add_u32_e32 v46, v46, v192
	v_add3_u32 v47, v133, v137, v141
	v_add3_u32 v47, v47, v145, v149
	v_add3_u32 v47, v47, v153, v157
	v_add3_u32 v47, v47, v161, v165
	v_add3_u32 v47, v47, v169, v173
	v_add3_u32 v47, v47, v177, v181
	v_add3_u32 v47, v47, v185, v189
	v_add_u32_e32 v47, v47, v193
	v_add3_u32 v48, v134, v138, v142
	v_add3_u32 v48, v48, v146, v150
	v_add3_u32 v48, v48, v154, v158
	v_add3_u32 v48, v48, v162, v166
	v_add3_u32 v48, v48, v170, v174
	v_add3_u32 v48, v48, v178, v182
	v_add3_u32 v48, v48, v186, v190
	v_add_u32_e32 v48, v48, v194
	v_add3_u32 v49, v135, v139, v143
	v_add3_u32 v49, v49, v147, v151
	v_add3_u32 v49, v49, v155, v159
	v_add3_u32 v49, v49, v163, v167
	v_add3_u32 v49, v49, v171, v175
	v_add3_u32 v49, v49, v179, v183
	v_add3_u32 v49, v49, v187, v191
	v_add_u32_e32 v49, v49, v195
	v_and_b32_e32 v50, 0xffff, v46
	v_lshrrev_b32_e32 v51, 16, v46
	v_and_b32_e32 v52, 0xffff, v47
	v_lshrrev_b32_e32 v53, 16, v47
	v_and_b32_e32 v54, 0xffff, v48
	v_lshrrev_b32_e32 v55, 16, v48
	v_and_b32_e32 v56, 0xffff, v49
	v_lshrrev_b32_e32 v57, 16, v49
	v_add_u32_e32 v30, v30, v50
	v_add_u32_e32 v31, v31, v51
	v_add_u32_e32 v32, v32, v52
	v_add_u32_e32 v33, v33, v53
	v_add_u32_e32 v34, v34, v54
	v_add_u32_e32 v35, v35, v55
	v_add_u32_e32 v36, v36, v56
	v_add_u32_e32 v37, v37, v57
	s_cmp_ge_i32 s15, 64
	s_cbranch_scc0 .Lbscat_nf_3
	v_add_u32_e32 v38, v38, v50
	v_add_u32_e32 v39, v39, v51
	v_add_u32_e32 v40, v40, v52
	v_add_u32_e32 v41, v41, v53
	v_add_u32_e32 v42, v42, v54
	v_add_u32_e32 v43, v43, v55
	v_add_u32_e32 v44, v44, v56
	v_add_u32_e32 v45, v45, v57
	s_branch .Lbscat_dn_3
.Lbscat_nf_3:
	s_cmp_gt_i32 s15, 48
	s_cbranch_scc0 .Lbscat_dn_3
	v_mov_b32_e32 v58, 0
	v_mov_b32_e32 v59, 0
	v_mov_b32_e32 v60, 0
	v_mov_b32_e32 v61, 0
	s_cmp_gt_i32 s15, 48
	s_cselect_b32 s16, -1, 0
	v_and_b32_e32 v62, s16, v132
	v_add_u32_e32 v58, v58, v62
	v_and_b32_e32 v62, s16, v133
	v_add_u32_e32 v59, v59, v62
	v_and_b32_e32 v62, s16, v134
	v_add_u32_e32 v60, v60, v62
	v_and_b32_e32 v62, s16, v135
	v_add_u32_e32 v61, v61, v62
	s_cmp_gt_i32 s15, 49
	s_cselect_b32 s16, -1, 0
	v_and_b32_e32 v62, s16, v136
	v_add_u32_e32 v58, v58, v62
	v_and_b32_e32 v62, s16, v137
	v_add_u32_e32 v59, v59, v62
	v_and_b32_e32 v62, s16, v138
	v_add_u32_e32 v60, v60, v62
	v_and_b32_e32 v62, s16, v139
	v_add_u32_e32 v61, v61, v62
	s_cmp_gt_i32 s15, 50
	s_cselect_b32 s16, -1, 0
	v_and_b32_e32 v62, s16, v140
	v_add_u32_e32 v58, v58, v62
	v_and_b32_e32 v62, s16, v141
	v_add_u32_e32 v59, v59, v62
	v_and_b32_e32 v62, s16, v142
	v_add_u32_e32 v60, v60, v62
	v_and_b32_e32 v62, s16, v143
	v_add_u32_e32 v61, v61, v62
	s_cmp_gt_i32 s15, 51
	s_cselect_b32 s16, -1, 0
	v_and_b32_e32 v62, s16, v144
	v_add_u32_e32 v58, v58, v62
	v_and_b32_e32 v62, s16, v145
	v_add_u32_e32 v59, v59, v62
	v_and_b32_e32 v62, s16, v146
	v_add_u32_e32 v60, v60, v62
	v_and_b32_e32 v62, s16, v147
	v_add_u32_e32 v61, v61, v62
	s_cmp_gt_i32 s15, 52
	s_cselect_b32 s16, -1, 0
	v_and_b32_e32 v62, s16, v148
	v_add_u32_e32 v58, v58, v62
	v_and_b32_e32 v62, s16, v149
	v_add_u32_e32 v59, v59, v62
	v_and_b32_e32 v62, s16, v150
	v_add_u32_e32 v60, v60, v62
	v_and_b32_e32 v62, s16, v151
	v_add_u32_e32 v61, v61, v62
	s_cmp_gt_i32 s15, 53
	s_cselect_b32 s16, -1, 0
	v_and_b32_e32 v62, s16, v152
	v_add_u32_e32 v58, v58, v62
	v_and_b32_e32 v62, s16, v153
	v_add_u32_e32 v59, v59, v62
	v_and_b32_e32 v62, s16, v154
	v_add_u32_e32 v60, v60, v62
	v_and_b32_e32 v62, s16, v155
	v_add_u32_e32 v61, v61, v62
	s_cmp_gt_i32 s15, 54
	s_cselect_b32 s16, -1, 0
	v_and_b32_e32 v62, s16, v156
	v_add_u32_e32 v58, v58, v62
	v_and_b32_e32 v62, s16, v157
	v_add_u32_e32 v59, v59, v62
	v_and_b32_e32 v62, s16, v158
	v_add_u32_e32 v60, v60, v62
	v_and_b32_e32 v62, s16, v159
	v_add_u32_e32 v61, v61, v62
	s_cmp_gt_i32 s15, 55
	s_cselect_b32 s16, -1, 0
	v_and_b32_e32 v62, s16, v160
	v_add_u32_e32 v58, v58, v62
	v_and_b32_e32 v62, s16, v161
	v_add_u32_e32 v59, v59, v62
	v_and_b32_e32 v62, s16, v162
	v_add_u32_e32 v60, v60, v62
	v_and_b32_e32 v62, s16, v163
	v_add_u32_e32 v61, v61, v62
	s_cmp_gt_i32 s15, 56
	s_cselect_b32 s16, -1, 0
	v_and_b32_e32 v62, s16, v164
	v_add_u32_e32 v58, v58, v62
	v_and_b32_e32 v62, s16, v165
	v_add_u32_e32 v59, v59, v62
	v_and_b32_e32 v62, s16, v166
	v_add_u32_e32 v60, v60, v62
	v_and_b32_e32 v62, s16, v167
	v_add_u32_e32 v61, v61, v62
	s_cmp_gt_i32 s15, 57
	s_cselect_b32 s16, -1, 0
	v_and_b32_e32 v62, s16, v168
	v_add_u32_e32 v58, v58, v62
	v_and_b32_e32 v62, s16, v169
	v_add_u32_e32 v59, v59, v62
	v_and_b32_e32 v62, s16, v170
	v_add_u32_e32 v60, v60, v62
	v_and_b32_e32 v62, s16, v171
	v_add_u32_e32 v61, v61, v62
	s_cmp_gt_i32 s15, 58
	s_cselect_b32 s16, -1, 0
	v_and_b32_e32 v62, s16, v172
	v_add_u32_e32 v58, v58, v62
	v_and_b32_e32 v62, s16, v173
	v_add_u32_e32 v59, v59, v62
	v_and_b32_e32 v62, s16, v174
	v_add_u32_e32 v60, v60, v62
	v_and_b32_e32 v62, s16, v175
	v_add_u32_e32 v61, v61, v62
	s_cmp_gt_i32 s15, 59
	s_cselect_b32 s16, -1, 0
	v_and_b32_e32 v62, s16, v176
	v_add_u32_e32 v58, v58, v62
	v_and_b32_e32 v62, s16, v177
	v_add_u32_e32 v59, v59, v62
	v_and_b32_e32 v62, s16, v178
	v_add_u32_e32 v60, v60, v62
	v_and_b32_e32 v62, s16, v179
	v_add_u32_e32 v61, v61, v62
	s_cmp_gt_i32 s15, 60
	s_cselect_b32 s16, -1, 0
	v_and_b32_e32 v62, s16, v180
	v_add_u32_e32 v58, v58, v62
	v_and_b32_e32 v62, s16, v181
	v_add_u32_e32 v59, v59, v62
	v_and_b32_e32 v62, s16, v182
	v_add_u32_e32 v60, v60, v62
	v_and_b32_e32 v62, s16, v183
	v_add_u32_e32 v61, v61, v62
	s_cmp_gt_i32 s15, 61
	s_cselect_b32 s16, -1, 0
	v_and_b32_e32 v62, s16, v184
	v_add_u32_e32 v58, v58, v62
	v_and_b32_e32 v62, s16, v185
	v_add_u32_e32 v59, v59, v62
	v_and_b32_e32 v62, s16, v186
	v_add_u32_e32 v60, v60, v62
	v_and_b32_e32 v62, s16, v187
	v_add_u32_e32 v61, v61, v62
	s_cmp_gt_i32 s15, 62
	s_cselect_b32 s16, -1, 0
	v_and_b32_e32 v62, s16, v188
	v_add_u32_e32 v58, v58, v62
	v_and_b32_e32 v62, s16, v189
	v_add_u32_e32 v59, v59, v62
	v_and_b32_e32 v62, s16, v190
	v_add_u32_e32 v60, v60, v62
	v_and_b32_e32 v62, s16, v191
	v_add_u32_e32 v61, v61, v62
	s_cmp_gt_i32 s15, 63
	s_cselect_b32 s16, -1, 0
	v_and_b32_e32 v62, s16, v192
	v_add_u32_e32 v58, v58, v62
	v_and_b32_e32 v62, s16, v193
	v_add_u32_e32 v59, v59, v62
	v_and_b32_e32 v62, s16, v194
	v_add_u32_e32 v60, v60, v62
	v_and_b32_e32 v62, s16, v195
	v_add_u32_e32 v61, v61, v62
	v_and_b32_e32 v50, 0xffff, v58
	v_lshrrev_b32_e32 v51, 16, v58
	v_and_b32_e32 v52, 0xffff, v59
	v_lshrrev_b32_e32 v53, 16, v59
	v_and_b32_e32 v54, 0xffff, v60
	v_lshrrev_b32_e32 v55, 16, v60
	v_and_b32_e32 v56, 0xffff, v61
	v_lshrrev_b32_e32 v57, 16, v61
	v_add_u32_e32 v38, v38, v50
	v_add_u32_e32 v39, v39, v51
	v_add_u32_e32 v40, v40, v52
	v_add_u32_e32 v41, v41, v53
	v_add_u32_e32 v42, v42, v54
	v_add_u32_e32 v43, v43, v55
	v_add_u32_e32 v44, v44, v56
	v_add_u32_e32 v45, v45, v57
.Lbscat_dn_3:
	ds_write_b128 v25, v[30:33] offset:6272
	ds_write_b128 v25, v[34:37] offset:6288
	ds_write_b128 v25, v[38:41]
	ds_write_b128 v25, v[42:45] offset:16
